# GEMM per-unit accumulator clearing: 128 v_mov_b32 replaced by 64 v_mov_b64 of zero (18 GEMM phases); on top of bias-hoist stack
# speedup vs baseline: 1.0035x; 1.0035x over previous
; template <class Epi, class Sched, bool ALIGN_EPI = true, bool SP2 = true, bool FP8 = false, bool GATHER = false>
; __device__ __forceinline__ void gemm_phase(LAS unsigned char* lds, const Dims g, const Sched& S, const Epi& E, const int wv) {
;     ...
; #pragma unroll
;         for (int a = 0; a < 2; ++a)
; #pragma unroll
;             for (int b = 0; b < 2; ++b)
; #pragma unroll
;                 for (int m = 0; m < 4; ++m)
; #pragma unroll
;                     for (int n = 0; n < 2; ++n) acc[a][b][m][n] = (f32x4){0.f, 0.f, 0.f, 0.f};
;         cur = nxt; cA = nA; cB = nB; ++ui;
.LBB0_232:
	s_add_u32 s5, s36, 0x100
	s_addc_u32 s17, s37, 0
	s_add_u32 s26, s26, 0x40080
	v_mov_b32_e32 v0, 0
	s_addc_u32 s27, s27, 0
	s_mov_b32 s21, -2
	v_mov_b64_e32 v[0:1], 0
	v_mov_b64_e32 v[2:3], 0
	v_mov_b64_e32 v[4:5], 0
	v_mov_b64_e32 v[6:7], 0
	v_mov_b64_e32 v[8:9], 0
	v_mov_b64_e32 v[10:11], 0
	v_mov_b64_e32 v[12:13], 0
	v_mov_b64_e32 v[14:15], 0
	v_mov_b64_e32 v[16:17], 0
	v_mov_b64_e32 v[18:19], 0
	v_mov_b64_e32 v[20:21], 0
	v_mov_b64_e32 v[22:23], 0
	v_mov_b64_e32 v[24:25], 0
	v_mov_b64_e32 v[26:27], 0
	v_mov_b64_e32 v[28:29], 0
	v_mov_b64_e32 v[30:31], 0
	v_mov_b64_e32 v[32:33], 0
	v_mov_b64_e32 v[34:35], 0
	v_mov_b64_e32 v[36:37], 0
	v_mov_b64_e32 v[38:39], 0
	v_mov_b64_e32 v[40:41], 0
	v_mov_b64_e32 v[42:43], 0
	v_mov_b64_e32 v[44:45], 0
	v_mov_b64_e32 v[46:47], 0
	v_mov_b64_e32 v[48:49], 0
	v_mov_b64_e32 v[50:51], 0
	v_mov_b64_e32 v[52:53], 0
	v_mov_b64_e32 v[54:55], 0
	v_mov_b64_e32 v[56:57], 0
	v_mov_b64_e32 v[58:59], 0
	v_mov_b64_e32 v[60:61], 0
	v_mov_b64_e32 v[62:63], 0
	v_mov_b64_e32 v[64:65], 0
	v_mov_b64_e32 v[66:67], 0
	v_mov_b64_e32 v[68:69], 0
	v_mov_b64_e32 v[70:71], 0
	v_mov_b64_e32 v[72:73], 0
	v_mov_b64_e32 v[74:75], 0
	v_mov_b64_e32 v[76:77], 0
	v_mov_b64_e32 v[78:79], 0
	v_mov_b64_e32 v[80:81], 0
	v_mov_b64_e32 v[82:83], 0
	v_mov_b64_e32 v[84:85], 0
	v_mov_b64_e32 v[86:87], 0
	v_mov_b64_e32 v[88:89], 0
	v_mov_b64_e32 v[90:91], 0
	v_mov_b64_e32 v[92:93], 0
	v_mov_b64_e32 v[94:95], 0
	v_mov_b64_e32 v[96:97], 0
	v_mov_b64_e32 v[98:99], 0
	v_mov_b64_e32 v[100:101], 0
	v_mov_b64_e32 v[102:103], 0
	v_mov_b64_e32 v[104:105], 0
	v_mov_b64_e32 v[106:107], 0
	v_mov_b64_e32 v[108:109], 0
	v_mov_b64_e32 v[110:111], 0
	v_mov_b64_e32 v[112:113], 0
	v_mov_b64_e32 v[114:115], 0
	v_mov_b64_e32 v[116:117], 0
	v_mov_b64_e32 v[118:119], 0
	v_mov_b64_e32 v[120:121], 0
	v_mov_b64_e32 v[122:123], 0
	v_mov_b64_e32 v[124:125], 0
	v_mov_b64_e32 v[126:127], 0

; template <class Epi, class Sched, bool ALIGN_EPI = true, bool SP2 = true, bool FP8 = false, bool GATHER = false>
; __device__ __forceinline__ void gemm_phase(LAS unsigned char* lds, const Dims g, const Sched& S, const Epi& E, const int wv) {
;     ...
; #pragma unroll
;         for (int a = 0; a < 2; ++a)
; #pragma unroll
;             for (int b = 0; b < 2; ++b)
; #pragma unroll
;                 for (int m = 0; m < 4; ++m)
; #pragma unroll
;                     for (int n = 0; n < 2; ++n) acc[a][b][m][n] = (f32x4){0.f, 0.f, 0.f, 0.f};
;         cur = nxt; cA = nA; cB = nB; ++ui;
.LBB0_411:
	v_mov_b32_e32 v0, 0
	s_mov_b64 s[40:41], 0
	s_mov_b64 s[36:37], -1
	s_mov_b64 s[38:39], 0
	v_mov_b64_e32 v[0:1], 0
	v_mov_b64_e32 v[2:3], 0
	v_mov_b64_e32 v[4:5], 0
	v_mov_b64_e32 v[6:7], 0
	v_mov_b64_e32 v[8:9], 0
	v_mov_b64_e32 v[10:11], 0
	v_mov_b64_e32 v[12:13], 0
	v_mov_b64_e32 v[14:15], 0
	v_mov_b64_e32 v[16:17], 0
	v_mov_b64_e32 v[18:19], 0
	v_mov_b64_e32 v[20:21], 0
	v_mov_b64_e32 v[22:23], 0
	v_mov_b64_e32 v[24:25], 0
	v_mov_b64_e32 v[26:27], 0
	v_mov_b64_e32 v[28:29], 0
	v_mov_b64_e32 v[30:31], 0
	v_mov_b64_e32 v[32:33], 0
	v_mov_b64_e32 v[34:35], 0
	v_mov_b64_e32 v[36:37], 0
	v_mov_b64_e32 v[38:39], 0
	v_mov_b64_e32 v[40:41], 0
	v_mov_b64_e32 v[42:43], 0
	v_mov_b64_e32 v[44:45], 0
	v_mov_b64_e32 v[46:47], 0
	v_mov_b64_e32 v[48:49], 0
	v_mov_b64_e32 v[50:51], 0
	v_mov_b64_e32 v[52:53], 0
	v_mov_b64_e32 v[54:55], 0
	v_mov_b64_e32 v[56:57], 0
	v_mov_b64_e32 v[58:59], 0
	v_mov_b64_e32 v[60:61], 0
	v_mov_b64_e32 v[62:63], 0
	v_mov_b64_e32 v[64:65], 0
	v_mov_b64_e32 v[66:67], 0
	v_mov_b64_e32 v[68:69], 0
	v_mov_b64_e32 v[70:71], 0
	v_mov_b64_e32 v[72:73], 0
	v_mov_b64_e32 v[74:75], 0
	v_mov_b64_e32 v[76:77], 0
	v_mov_b64_e32 v[78:79], 0
	v_mov_b64_e32 v[80:81], 0
	v_mov_b64_e32 v[82:83], 0
	v_mov_b64_e32 v[84:85], 0
	v_mov_b64_e32 v[86:87], 0
	v_mov_b64_e32 v[88:89], 0
	v_mov_b64_e32 v[90:91], 0
	v_mov_b64_e32 v[92:93], 0
	v_mov_b64_e32 v[94:95], 0
	v_mov_b64_e32 v[96:97], 0
	v_mov_b64_e32 v[98:99], 0
	v_mov_b64_e32 v[100:101], 0
	v_mov_b64_e32 v[102:103], 0
	v_mov_b64_e32 v[104:105], 0
	v_mov_b64_e32 v[106:107], 0
	v_mov_b64_e32 v[108:109], 0
	v_mov_b64_e32 v[110:111], 0
	v_mov_b64_e32 v[112:113], 0
	v_mov_b64_e32 v[114:115], 0
	v_mov_b64_e32 v[116:117], 0
	v_mov_b64_e32 v[118:119], 0
	v_mov_b64_e32 v[120:121], 0
	v_mov_b64_e32 v[122:123], 0
	v_mov_b64_e32 v[124:125], 0
	v_mov_b64_e32 v[126:127], 0

; template <class Epi, class Sched, bool ALIGN_EPI = true, bool SP2 = true, bool FP8 = false, bool GATHER = false>
; __device__ __forceinline__ void gemm_phase(LAS unsigned char* lds, const Dims g, const Sched& S, const Epi& E, const int wv) {
;     ...
; #pragma unroll
;         for (int a = 0; a < 2; ++a)
; #pragma unroll
;             for (int b = 0; b < 2; ++b)
; #pragma unroll
;                 for (int m = 0; m < 4; ++m)
; #pragma unroll
;                     for (int n = 0; n < 2; ++n) acc[a][b][m][n] = (f32x4){0.f, 0.f, 0.f, 0.f};
;         cur = nxt; cA = nA; cB = nB; ++ui;
.LBB0_744:
	s_add_u32 s5, s46, 0x100
	s_addc_u32 s37, s47, 0
	s_add_u32 s39, s44, 0x100
	s_addc_u32 s81, s45, 0
	s_add_u32 s44, s44, 0x20080
	v_mov_b32_e32 v0, 0
	s_addc_u32 s45, s45, 0
	s_mov_b32 s82, -2
	v_mov_b64_e32 v[0:1], 0
	v_mov_b64_e32 v[2:3], 0
	v_mov_b64_e32 v[4:5], 0
	v_mov_b64_e32 v[6:7], 0
	v_mov_b64_e32 v[8:9], 0
	v_mov_b64_e32 v[10:11], 0
	v_mov_b64_e32 v[12:13], 0
	v_mov_b64_e32 v[14:15], 0
	v_mov_b64_e32 v[16:17], 0
	v_mov_b64_e32 v[18:19], 0
	v_mov_b64_e32 v[20:21], 0
	v_mov_b64_e32 v[22:23], 0
	v_mov_b64_e32 v[24:25], 0
	v_mov_b64_e32 v[26:27], 0
	v_mov_b64_e32 v[28:29], 0
	v_mov_b64_e32 v[30:31], 0
	v_mov_b64_e32 v[32:33], 0
	v_mov_b64_e32 v[34:35], 0
	v_mov_b64_e32 v[36:37], 0
	v_mov_b64_e32 v[38:39], 0
	v_mov_b64_e32 v[40:41], 0
	v_mov_b64_e32 v[42:43], 0
	v_mov_b64_e32 v[44:45], 0
	v_mov_b64_e32 v[46:47], 0
	v_mov_b64_e32 v[48:49], 0
	v_mov_b64_e32 v[50:51], 0
	v_mov_b64_e32 v[52:53], 0
	v_mov_b64_e32 v[54:55], 0
	v_mov_b64_e32 v[56:57], 0
	v_mov_b64_e32 v[58:59], 0
	v_mov_b64_e32 v[60:61], 0
	v_mov_b64_e32 v[62:63], 0
	v_mov_b64_e32 v[64:65], 0
	v_mov_b64_e32 v[66:67], 0
	v_mov_b64_e32 v[68:69], 0
	v_mov_b64_e32 v[70:71], 0
	v_mov_b64_e32 v[72:73], 0
	v_mov_b64_e32 v[74:75], 0
	v_mov_b64_e32 v[76:77], 0
	v_mov_b64_e32 v[78:79], 0
	v_mov_b64_e32 v[80:81], 0
	v_mov_b64_e32 v[82:83], 0
	v_mov_b64_e32 v[84:85], 0
	v_mov_b64_e32 v[86:87], 0
	v_mov_b64_e32 v[88:89], 0
	v_mov_b64_e32 v[90:91], 0
	v_mov_b64_e32 v[92:93], 0
	v_mov_b64_e32 v[94:95], 0
	v_mov_b64_e32 v[96:97], 0
	v_mov_b64_e32 v[98:99], 0
	v_mov_b64_e32 v[100:101], 0
	v_mov_b64_e32 v[102:103], 0
	v_mov_b64_e32 v[104:105], 0
	v_mov_b64_e32 v[106:107], 0
	v_mov_b64_e32 v[108:109], 0
	v_mov_b64_e32 v[110:111], 0
	v_mov_b64_e32 v[112:113], 0
	v_mov_b64_e32 v[114:115], 0
	v_mov_b64_e32 v[116:117], 0
	v_mov_b64_e32 v[118:119], 0
	v_mov_b64_e32 v[120:121], 0
	v_mov_b64_e32 v[122:123], 0
	v_mov_b64_e32 v[124:125], 0
	v_mov_b64_e32 v[126:127], 0

; template <class Epi, class Sched, bool ALIGN_EPI = true, bool SP2 = true, bool FP8 = false, bool GATHER = false>
; __device__ __forceinline__ void gemm_phase(LAS unsigned char* lds, const Dims g, const Sched& S, const Epi& E, const int wv) {
;     ...
; #pragma unroll
;         for (int a = 0; a < 2; ++a)
; #pragma unroll
;             for (int b = 0; b < 2; ++b)
; #pragma unroll
;                 for (int m = 0; m < 4; ++m)
; #pragma unroll
;                     for (int n = 0; n < 2; ++n) acc[a][b][m][n] = (f32x4){0.f, 0.f, 0.f, 0.f};
;         cur = nxt; cA = nA; cB = nB; ++ui;
.LBB0_1425:
	s_and_b64 s[44:45], s[26:27], exec
	s_cselect_b32 s44, s76, s81
	s_cselect_b32 s39, s3, s41
	s_cselect_b32 s78, s2, s40
	s_cselect_b32 s79, s25, s43
	s_cselect_b32 s80, s24, s42
	s_lshl_b32 s44, s44, 10
	s_add_i32 s81, s44, 0
	s_add_i32 s81, s81, 0x21500
	s_add_u32 s82, s42, 0x100
	v_mov_b32_e32 v64, 0
	s_addc_u32 s83, s43, 0
	s_mov_b32 s84, -2
	v_mov_b64_e32 v[64:65], 0
	v_mov_b64_e32 v[66:67], 0
	v_mov_b64_e32 v[68:69], 0
	v_mov_b64_e32 v[70:71], 0
	v_mov_b64_e32 v[72:73], 0
	v_mov_b64_e32 v[74:75], 0
	v_mov_b64_e32 v[76:77], 0
	v_mov_b64_e32 v[78:79], 0
	v_mov_b64_e32 v[80:81], 0
	v_mov_b64_e32 v[82:83], 0
	v_mov_b64_e32 v[84:85], 0
	v_mov_b64_e32 v[86:87], 0
	v_mov_b64_e32 v[88:89], 0
	v_mov_b64_e32 v[90:91], 0
	v_mov_b64_e32 v[92:93], 0
	v_mov_b64_e32 v[94:95], 0
	v_mov_b64_e32 v[96:97], 0
	v_mov_b64_e32 v[98:99], 0
	v_mov_b64_e32 v[100:101], 0
	v_mov_b64_e32 v[102:103], 0
	v_mov_b64_e32 v[104:105], 0
	v_mov_b64_e32 v[106:107], 0
	v_mov_b64_e32 v[108:109], 0
	v_mov_b64_e32 v[110:111], 0
	v_mov_b64_e32 v[112:113], 0
	v_mov_b64_e32 v[114:115], 0
	v_mov_b64_e32 v[116:117], 0
	v_mov_b64_e32 v[118:119], 0
	v_mov_b64_e32 v[120:121], 0
	v_mov_b64_e32 v[122:123], 0
	v_mov_b64_e32 v[124:125], 0
	v_mov_b64_e32 v[126:127], 0
	v_mov_b64_e32 v[128:129], 0
	v_mov_b64_e32 v[130:131], 0
	v_mov_b64_e32 v[132:133], 0
	v_mov_b64_e32 v[134:135], 0
	v_mov_b64_e32 v[136:137], 0
	v_mov_b64_e32 v[138:139], 0
	v_mov_b64_e32 v[140:141], 0
	v_mov_b64_e32 v[142:143], 0
	v_mov_b64_e32 v[144:145], 0
	v_mov_b64_e32 v[146:147], 0
	v_mov_b64_e32 v[148:149], 0
	v_mov_b64_e32 v[150:151], 0
	v_mov_b64_e32 v[152:153], 0
	v_mov_b64_e32 v[154:155], 0
	v_mov_b64_e32 v[156:157], 0
	v_mov_b64_e32 v[158:159], 0
	v_mov_b64_e32 v[160:161], 0
	v_mov_b64_e32 v[162:163], 0
	v_mov_b64_e32 v[164:165], 0
	v_mov_b64_e32 v[166:167], 0
	v_mov_b64_e32 v[168:169], 0
	v_mov_b64_e32 v[170:171], 0
	v_mov_b64_e32 v[172:173], 0
	v_mov_b64_e32 v[174:175], 0
	v_mov_b64_e32 v[176:177], 0
	v_mov_b64_e32 v[178:179], 0
	v_mov_b64_e32 v[180:181], 0
	v_mov_b64_e32 v[182:183], 0
	v_mov_b64_e32 v[184:185], 0
	v_mov_b64_e32 v[186:187], 0
	v_mov_b64_e32 v[188:189], 0
	v_mov_b64_e32 v[190:191], 0
	s_branch .LBB0_1427

; template <class Epi, class Sched, bool ALIGN_EPI = true, bool SP2 = true, bool FP8 = false, bool GATHER = false>
; __device__ __forceinline__ void gemm_phase(LAS unsigned char* lds, const Dims g, const Sched& S, const Epi& E, const int wv) {
;     ...
; #pragma unroll
;         for (int a = 0; a < 2; ++a)
; #pragma unroll
;             for (int b = 0; b < 2; ++b)
; #pragma unroll
;                 for (int m = 0; m < 4; ++m)
; #pragma unroll
;                     for (int n = 0; n < 2; ++n) acc[a][b][m][n] = (f32x4){0.f, 0.f, 0.f, 0.f};
;         cur = nxt; cA = nA; cB = nB; ++ui;
.LBB0_1527:
	s_and_b64 s[48:49], s[36:37], exec
	s_cselect_b32 s39, s25, s45
	s_cselect_b32 s43, s24, s44
	s_cselect_b32 s54, s27, s47
	s_cselect_b32 s55, s26, s46
	s_add_u32 s84, s46, 0x100
	v_mov_b32_e32 v0, 0
	s_addc_u32 s85, s47, 0
	s_mov_b32 s86, -2
	v_mov_b64_e32 v[0:1], 0
	v_mov_b64_e32 v[2:3], 0
	v_mov_b64_e32 v[4:5], 0
	v_mov_b64_e32 v[6:7], 0
	v_mov_b64_e32 v[8:9], 0
	v_mov_b64_e32 v[10:11], 0
	v_mov_b64_e32 v[12:13], 0
	v_mov_b64_e32 v[14:15], 0
	v_mov_b64_e32 v[16:17], 0
	v_mov_b64_e32 v[18:19], 0
	v_mov_b64_e32 v[20:21], 0
	v_mov_b64_e32 v[22:23], 0
	v_mov_b64_e32 v[24:25], 0
	v_mov_b64_e32 v[26:27], 0
	v_mov_b64_e32 v[28:29], 0
	v_mov_b64_e32 v[30:31], 0
	v_mov_b64_e32 v[32:33], 0
	v_mov_b64_e32 v[34:35], 0
	v_mov_b64_e32 v[36:37], 0
	v_mov_b64_e32 v[38:39], 0
	v_mov_b64_e32 v[40:41], 0
	v_mov_b64_e32 v[42:43], 0
	v_mov_b64_e32 v[44:45], 0
	v_mov_b64_e32 v[46:47], 0
	v_mov_b64_e32 v[48:49], 0
	v_mov_b64_e32 v[50:51], 0
	v_mov_b64_e32 v[52:53], 0
	v_mov_b64_e32 v[54:55], 0
	v_mov_b64_e32 v[56:57], 0
	v_mov_b64_e32 v[58:59], 0
	v_mov_b64_e32 v[60:61], 0
	v_mov_b64_e32 v[62:63], 0
	v_mov_b64_e32 v[64:65], 0
	v_mov_b64_e32 v[66:67], 0
	v_mov_b64_e32 v[68:69], 0
	v_mov_b64_e32 v[70:71], 0
	v_mov_b64_e32 v[72:73], 0
	v_mov_b64_e32 v[74:75], 0
	v_mov_b64_e32 v[76:77], 0
	v_mov_b64_e32 v[78:79], 0
	v_mov_b64_e32 v[80:81], 0
	v_mov_b64_e32 v[82:83], 0
	v_mov_b64_e32 v[84:85], 0
	v_mov_b64_e32 v[86:87], 0
	v_mov_b64_e32 v[88:89], 0
	v_mov_b64_e32 v[90:91], 0
	v_mov_b64_e32 v[92:93], 0
	v_mov_b64_e32 v[94:95], 0
	v_mov_b64_e32 v[96:97], 0
	v_mov_b64_e32 v[98:99], 0
	v_mov_b64_e32 v[100:101], 0
	v_mov_b64_e32 v[102:103], 0
	v_mov_b64_e32 v[104:105], 0
	v_mov_b64_e32 v[106:107], 0
	v_mov_b64_e32 v[108:109], 0
	v_mov_b64_e32 v[110:111], 0
	v_mov_b64_e32 v[112:113], 0
	v_mov_b64_e32 v[114:115], 0
	v_mov_b64_e32 v[116:117], 0
	v_mov_b64_e32 v[118:119], 0
	v_mov_b64_e32 v[120:121], 0
	v_mov_b64_e32 v[122:123], 0
	v_mov_b64_e32 v[124:125], 0
	v_mov_b64_e32 v[126:127], 0

; template <class Epi, class Sched, bool ALIGN_EPI = true, bool SP2 = true, bool FP8 = false, bool GATHER = false>
; __device__ __forceinline__ void gemm_phase(LAS unsigned char* lds, const Dims g, const Sched& S, const Epi& E, const int wv) {
;     ...
; #pragma unroll
;         for (int a = 0; a < 2; ++a)
; #pragma unroll
;             for (int b = 0; b < 2; ++b)
; #pragma unroll
;                 for (int m = 0; m < 4; ++m)
; #pragma unroll
;                     for (int n = 0; n < 2; ++n) acc[a][b][m][n] = (f32x4){0.f, 0.f, 0.f, 0.f};
;         cur = nxt; cA = nA; cB = nB; ++ui;
.LBB0_1669:
	s_add_u32 s5, s42, 0x100
	v_mov_b32_e32 v0, 0
	s_addc_u32 s6, s43, 0
	s_mov_b32 s25, -2
	v_mov_b64_e32 v[0:1], 0
	v_mov_b64_e32 v[2:3], 0
	v_mov_b64_e32 v[4:5], 0
	v_mov_b64_e32 v[6:7], 0
	v_mov_b64_e32 v[8:9], 0
	v_mov_b64_e32 v[10:11], 0
	v_mov_b64_e32 v[12:13], 0
	v_mov_b64_e32 v[14:15], 0
	v_mov_b64_e32 v[16:17], 0
	v_mov_b64_e32 v[18:19], 0
	v_mov_b64_e32 v[20:21], 0
	v_mov_b64_e32 v[22:23], 0
	v_mov_b64_e32 v[24:25], 0
	v_mov_b64_e32 v[26:27], 0
	v_mov_b64_e32 v[28:29], 0
	v_mov_b64_e32 v[30:31], 0
	v_mov_b64_e32 v[32:33], 0
	v_mov_b64_e32 v[34:35], 0
	v_mov_b64_e32 v[36:37], 0
	v_mov_b64_e32 v[38:39], 0
	v_mov_b64_e32 v[40:41], 0
	v_mov_b64_e32 v[42:43], 0
	v_mov_b64_e32 v[44:45], 0
	v_mov_b64_e32 v[46:47], 0
	v_mov_b64_e32 v[48:49], 0
	v_mov_b64_e32 v[50:51], 0
	v_mov_b64_e32 v[52:53], 0
	v_mov_b64_e32 v[54:55], 0
	v_mov_b64_e32 v[56:57], 0
	v_mov_b64_e32 v[58:59], 0
	v_mov_b64_e32 v[60:61], 0
	v_mov_b64_e32 v[62:63], 0
	v_mov_b64_e32 v[64:65], 0
	v_mov_b64_e32 v[66:67], 0
	v_mov_b64_e32 v[68:69], 0
	v_mov_b64_e32 v[70:71], 0
	v_mov_b64_e32 v[72:73], 0
	v_mov_b64_e32 v[74:75], 0
	v_mov_b64_e32 v[76:77], 0
	v_mov_b64_e32 v[78:79], 0
	v_mov_b64_e32 v[80:81], 0
	v_mov_b64_e32 v[82:83], 0
	v_mov_b64_e32 v[84:85], 0
	v_mov_b64_e32 v[86:87], 0
	v_mov_b64_e32 v[88:89], 0
	v_mov_b64_e32 v[90:91], 0
	v_mov_b64_e32 v[92:93], 0
	v_mov_b64_e32 v[94:95], 0
	v_mov_b64_e32 v[96:97], 0
	v_mov_b64_e32 v[98:99], 0
	v_mov_b64_e32 v[100:101], 0
	v_mov_b64_e32 v[102:103], 0
	v_mov_b64_e32 v[104:105], 0
	v_mov_b64_e32 v[106:107], 0
	v_mov_b64_e32 v[108:109], 0
	v_mov_b64_e32 v[110:111], 0
	v_mov_b64_e32 v[112:113], 0
	v_mov_b64_e32 v[114:115], 0
	v_mov_b64_e32 v[116:117], 0
	v_mov_b64_e32 v[118:119], 0
	v_mov_b64_e32 v[120:121], 0
	v_mov_b64_e32 v[122:123], 0
	v_mov_b64_e32 v[124:125], 0
	v_mov_b64_e32 v[126:127], 0

; template <class Epi, class Sched, bool ALIGN_EPI = true, bool SP2 = true, bool FP8 = false, bool GATHER = false>
; __device__ __forceinline__ void gemm_phase(LAS unsigned char* lds, const Dims g, const Sched& S, const Epi& E, const int wv) {
;     ...
; #pragma unroll
;         for (int a = 0; a < 2; ++a)
; #pragma unroll
;             for (int b = 0; b < 2; ++b)
; #pragma unroll
;                 for (int m = 0; m < 4; ++m)
; #pragma unroll
;                     for (int n = 0; n < 2; ++n) acc[a][b][m][n] = (f32x4){0.f, 0.f, 0.f, 0.f};
;         cur = nxt; cA = nA; cB = nB; ++ui;
.LBB0_1912:
	s_add_u32 s23, s42, 0x100
	s_addc_u32 s25, s43, 0
	s_add_u32 s80, s40, 0x100
	s_addc_u32 s81, s41, 0
	s_add_u32 s40, s40, 0x40080
	v_mov_b32_e32 v0, 0
	s_addc_u32 s41, s41, 0
	s_mov_b32 s82, -2
	v_mov_b64_e32 v[0:1], 0
	v_mov_b64_e32 v[2:3], 0
	v_mov_b64_e32 v[4:5], 0
	v_mov_b64_e32 v[6:7], 0
	v_mov_b64_e32 v[8:9], 0
	v_mov_b64_e32 v[10:11], 0
	v_mov_b64_e32 v[12:13], 0
	v_mov_b64_e32 v[14:15], 0
	v_mov_b64_e32 v[16:17], 0
	v_mov_b64_e32 v[18:19], 0
	v_mov_b64_e32 v[20:21], 0
	v_mov_b64_e32 v[22:23], 0
	v_mov_b64_e32 v[24:25], 0
	v_mov_b64_e32 v[26:27], 0
	v_mov_b64_e32 v[28:29], 0
	v_mov_b64_e32 v[30:31], 0
	v_mov_b64_e32 v[32:33], 0
	v_mov_b64_e32 v[34:35], 0
	v_mov_b64_e32 v[36:37], 0
	v_mov_b64_e32 v[38:39], 0
	v_mov_b64_e32 v[40:41], 0
	v_mov_b64_e32 v[42:43], 0
	v_mov_b64_e32 v[44:45], 0
	v_mov_b64_e32 v[46:47], 0
	v_mov_b64_e32 v[48:49], 0
	v_mov_b64_e32 v[50:51], 0
	v_mov_b64_e32 v[52:53], 0
	v_mov_b64_e32 v[54:55], 0
	v_mov_b64_e32 v[56:57], 0
	v_mov_b64_e32 v[58:59], 0
	v_mov_b64_e32 v[60:61], 0
	v_mov_b64_e32 v[62:63], 0
	v_mov_b64_e32 v[64:65], 0
	v_mov_b64_e32 v[66:67], 0
	v_mov_b64_e32 v[68:69], 0
	v_mov_b64_e32 v[70:71], 0
	v_mov_b64_e32 v[72:73], 0
	v_mov_b64_e32 v[74:75], 0
	v_mov_b64_e32 v[76:77], 0
	v_mov_b64_e32 v[78:79], 0
	v_mov_b64_e32 v[80:81], 0
	v_mov_b64_e32 v[82:83], 0
	v_mov_b64_e32 v[84:85], 0
	v_mov_b64_e32 v[86:87], 0
	v_mov_b64_e32 v[88:89], 0
	v_mov_b64_e32 v[90:91], 0
	v_mov_b64_e32 v[92:93], 0
	v_mov_b64_e32 v[94:95], 0
	v_mov_b64_e32 v[96:97], 0
	v_mov_b64_e32 v[98:99], 0
	v_mov_b64_e32 v[100:101], 0
	v_mov_b64_e32 v[102:103], 0
	v_mov_b64_e32 v[104:105], 0
	v_mov_b64_e32 v[106:107], 0
	v_mov_b64_e32 v[108:109], 0
	v_mov_b64_e32 v[110:111], 0
	v_mov_b64_e32 v[112:113], 0
	v_mov_b64_e32 v[114:115], 0
	v_mov_b64_e32 v[116:117], 0
	v_mov_b64_e32 v[118:119], 0
	v_mov_b64_e32 v[120:121], 0
	v_mov_b64_e32 v[122:123], 0
	v_mov_b64_e32 v[124:125], 0
	v_mov_b64_e32 v[126:127], 0

; template <class Epi, class Sched, bool ALIGN_EPI = true, bool SP2 = true, bool FP8 = false, bool GATHER = false>
; __device__ __forceinline__ void gemm_phase(LAS unsigned char* lds, const Dims g, const Sched& S, const Epi& E, const int wv) {
;     ...
; #pragma unroll
;         for (int a = 0; a < 2; ++a)
; #pragma unroll
;             for (int b = 0; b < 2; ++b)
; #pragma unroll
;                 for (int m = 0; m < 4; ++m)
; #pragma unroll
;                     for (int n = 0; n < 2; ++n) acc[a][b][m][n] = (f32x4){0.f, 0.f, 0.f, 0.f};
;         cur = nxt; cA = nA; cB = nB; ++ui;
.LBB0_2529:
	s_and_b64 s[42:43], s[24:25], exec
	s_cselect_b32 s42, s76, s81
	s_cselect_b32 s37, s3, s39
	s_cselect_b32 s78, s2, s38
	s_cselect_b32 s79, s23, s41
	s_cselect_b32 s80, s22, s40
	s_lshl_b32 s42, s42, 10
	s_add_i32 s81, s42, 0
	s_add_i32 s81, s81, 0x21500
	s_add_u32 s82, s40, 0x100
	v_mov_b32_e32 v64, 0
	s_addc_u32 s83, s41, 0
	s_mov_b32 s84, -2
	v_mov_b64_e32 v[64:65], 0
	v_mov_b64_e32 v[66:67], 0
	v_mov_b64_e32 v[68:69], 0
	v_mov_b64_e32 v[70:71], 0
	v_mov_b64_e32 v[72:73], 0
	v_mov_b64_e32 v[74:75], 0
	v_mov_b64_e32 v[76:77], 0
	v_mov_b64_e32 v[78:79], 0
	v_mov_b64_e32 v[80:81], 0
	v_mov_b64_e32 v[82:83], 0
	v_mov_b64_e32 v[84:85], 0
	v_mov_b64_e32 v[86:87], 0
	v_mov_b64_e32 v[88:89], 0
	v_mov_b64_e32 v[90:91], 0
	v_mov_b64_e32 v[92:93], 0
	v_mov_b64_e32 v[94:95], 0
	v_mov_b64_e32 v[96:97], 0
	v_mov_b64_e32 v[98:99], 0
	v_mov_b64_e32 v[100:101], 0
	v_mov_b64_e32 v[102:103], 0
	v_mov_b64_e32 v[104:105], 0
	v_mov_b64_e32 v[106:107], 0
	v_mov_b64_e32 v[108:109], 0
	v_mov_b64_e32 v[110:111], 0
	v_mov_b64_e32 v[112:113], 0
	v_mov_b64_e32 v[114:115], 0
	v_mov_b64_e32 v[116:117], 0
	v_mov_b64_e32 v[118:119], 0
	v_mov_b64_e32 v[120:121], 0
	v_mov_b64_e32 v[122:123], 0
	v_mov_b64_e32 v[124:125], 0
	v_mov_b64_e32 v[126:127], 0
	v_mov_b64_e32 v[128:129], 0
	v_mov_b64_e32 v[130:131], 0
	v_mov_b64_e32 v[132:133], 0
	v_mov_b64_e32 v[134:135], 0
	v_mov_b64_e32 v[136:137], 0
	v_mov_b64_e32 v[138:139], 0
	v_mov_b64_e32 v[140:141], 0
	v_mov_b64_e32 v[142:143], 0
	v_mov_b64_e32 v[144:145], 0
	v_mov_b64_e32 v[146:147], 0
	v_mov_b64_e32 v[148:149], 0
	v_mov_b64_e32 v[150:151], 0
	v_mov_b64_e32 v[152:153], 0
	v_mov_b64_e32 v[154:155], 0
	v_mov_b64_e32 v[156:157], 0
	v_mov_b64_e32 v[158:159], 0
	v_mov_b64_e32 v[160:161], 0
	v_mov_b64_e32 v[162:163], 0
	v_mov_b64_e32 v[164:165], 0
	v_mov_b64_e32 v[166:167], 0
	v_mov_b64_e32 v[168:169], 0
	v_mov_b64_e32 v[170:171], 0
	v_mov_b64_e32 v[172:173], 0
	v_mov_b64_e32 v[174:175], 0
	v_mov_b64_e32 v[176:177], 0
	v_mov_b64_e32 v[178:179], 0
	v_mov_b64_e32 v[180:181], 0
	v_mov_b64_e32 v[182:183], 0
	v_mov_b64_e32 v[184:185], 0
	v_mov_b64_e32 v[186:187], 0
	v_mov_b64_e32 v[188:189], 0
	v_mov_b64_e32 v[190:191], 0
	s_branch .LBB0_2531

; template <class Epi, class Sched, bool ALIGN_EPI = true, bool SP2 = true, bool FP8 = false, bool GATHER = false>
; __device__ __forceinline__ void gemm_phase(LAS unsigned char* lds, const Dims g, const Sched& S, const Epi& E, const int wv) {
;     ...
; #pragma unroll
;         for (int a = 0; a < 2; ++a)
; #pragma unroll
;             for (int b = 0; b < 2; ++b)
; #pragma unroll
;                 for (int m = 0; m < 4; ++m)
; #pragma unroll
;                     for (int n = 0; n < 2; ++n) acc[a][b][m][n] = (f32x4){0.f, 0.f, 0.f, 0.f};
;         cur = nxt; cA = nA; cB = nB; ++ui;
.LBB0_2631:
	s_and_b64 s[46:47], s[26:27], exec
	s_cselect_b32 s37, s23, s43
	s_cselect_b32 s41, s22, s42
	s_cselect_b32 s52, s25, s45
	s_cselect_b32 s53, s24, s44
	s_add_u32 s84, s44, 0x100
	v_mov_b32_e32 v0, 0
	s_addc_u32 s85, s45, 0
	s_mov_b32 s86, -2
	v_mov_b64_e32 v[0:1], 0
	v_mov_b64_e32 v[2:3], 0
	v_mov_b64_e32 v[4:5], 0
	v_mov_b64_e32 v[6:7], 0
	v_mov_b64_e32 v[8:9], 0
	v_mov_b64_e32 v[10:11], 0
	v_mov_b64_e32 v[12:13], 0
	v_mov_b64_e32 v[14:15], 0
	v_mov_b64_e32 v[16:17], 0
	v_mov_b64_e32 v[18:19], 0
	v_mov_b64_e32 v[20:21], 0
	v_mov_b64_e32 v[22:23], 0
	v_mov_b64_e32 v[24:25], 0
	v_mov_b64_e32 v[26:27], 0
	v_mov_b64_e32 v[28:29], 0
	v_mov_b64_e32 v[30:31], 0
	v_mov_b64_e32 v[32:33], 0
	v_mov_b64_e32 v[34:35], 0
	v_mov_b64_e32 v[36:37], 0
	v_mov_b64_e32 v[38:39], 0
	v_mov_b64_e32 v[40:41], 0
	v_mov_b64_e32 v[42:43], 0
	v_mov_b64_e32 v[44:45], 0
	v_mov_b64_e32 v[46:47], 0
	v_mov_b64_e32 v[48:49], 0
	v_mov_b64_e32 v[50:51], 0
	v_mov_b64_e32 v[52:53], 0
	v_mov_b64_e32 v[54:55], 0
	v_mov_b64_e32 v[56:57], 0
	v_mov_b64_e32 v[58:59], 0
	v_mov_b64_e32 v[60:61], 0
	v_mov_b64_e32 v[62:63], 0
	v_mov_b64_e32 v[64:65], 0
	v_mov_b64_e32 v[66:67], 0
	v_mov_b64_e32 v[68:69], 0
	v_mov_b64_e32 v[70:71], 0
	v_mov_b64_e32 v[72:73], 0
	v_mov_b64_e32 v[74:75], 0
	v_mov_b64_e32 v[76:77], 0
	v_mov_b64_e32 v[78:79], 0
	v_mov_b64_e32 v[80:81], 0
	v_mov_b64_e32 v[82:83], 0
	v_mov_b64_e32 v[84:85], 0
	v_mov_b64_e32 v[86:87], 0
	v_mov_b64_e32 v[88:89], 0
	v_mov_b64_e32 v[90:91], 0
	v_mov_b64_e32 v[92:93], 0
	v_mov_b64_e32 v[94:95], 0
	v_mov_b64_e32 v[96:97], 0
	v_mov_b64_e32 v[98:99], 0
	v_mov_b64_e32 v[100:101], 0
	v_mov_b64_e32 v[102:103], 0
	v_mov_b64_e32 v[104:105], 0
	v_mov_b64_e32 v[106:107], 0
	v_mov_b64_e32 v[108:109], 0
	v_mov_b64_e32 v[110:111], 0
	v_mov_b64_e32 v[112:113], 0
	v_mov_b64_e32 v[114:115], 0
	v_mov_b64_e32 v[116:117], 0
	v_mov_b64_e32 v[118:119], 0
	v_mov_b64_e32 v[120:121], 0
	v_mov_b64_e32 v[122:123], 0
	v_mov_b64_e32 v[124:125], 0
	v_mov_b64_e32 v[126:127], 0

; template <class Epi, class Sched, bool ALIGN_EPI = true, bool SP2 = true, bool FP8 = false, bool GATHER = false>
; __device__ __forceinline__ void gemm_phase(LAS unsigned char* lds, const Dims g, const Sched& S, const Epi& E, const int wv) {
;     ...
; #pragma unroll
;         for (int a = 0; a < 2; ++a)
; #pragma unroll
;             for (int b = 0; b < 2; ++b)
; #pragma unroll
;                 for (int m = 0; m < 4; ++m)
; #pragma unroll
;                     for (int n = 0; n < 2; ++n) acc[a][b][m][n] = (f32x4){0.f, 0.f, 0.f, 0.f};
;         cur = nxt; cA = nA; cB = nB; ++ui;
.LBB0_3283:
	s_add_u32 s23, s42, 0x100
	s_addc_u32 s25, s43, 0
	s_add_u32 s80, s40, 0x100
	s_addc_u32 s81, s41, 0
	s_add_u32 s40, s40, 0x20080
	v_mov_b32_e32 v0, 0
	s_addc_u32 s41, s41, 0
	s_mov_b32 s82, -2
	v_mov_b64_e32 v[0:1], 0
	v_mov_b64_e32 v[2:3], 0
	v_mov_b64_e32 v[4:5], 0
	v_mov_b64_e32 v[6:7], 0
	v_mov_b64_e32 v[8:9], 0
	v_mov_b64_e32 v[10:11], 0
	v_mov_b64_e32 v[12:13], 0
	v_mov_b64_e32 v[14:15], 0
	v_mov_b64_e32 v[16:17], 0
	v_mov_b64_e32 v[18:19], 0
	v_mov_b64_e32 v[20:21], 0
	v_mov_b64_e32 v[22:23], 0
	v_mov_b64_e32 v[24:25], 0
	v_mov_b64_e32 v[26:27], 0
	v_mov_b64_e32 v[28:29], 0
	v_mov_b64_e32 v[30:31], 0
	v_mov_b64_e32 v[32:33], 0
	v_mov_b64_e32 v[34:35], 0
	v_mov_b64_e32 v[36:37], 0
	v_mov_b64_e32 v[38:39], 0
	v_mov_b64_e32 v[40:41], 0
	v_mov_b64_e32 v[42:43], 0
	v_mov_b64_e32 v[44:45], 0
	v_mov_b64_e32 v[46:47], 0
	v_mov_b64_e32 v[48:49], 0
	v_mov_b64_e32 v[50:51], 0
	v_mov_b64_e32 v[52:53], 0
	v_mov_b64_e32 v[54:55], 0
	v_mov_b64_e32 v[56:57], 0
	v_mov_b64_e32 v[58:59], 0
	v_mov_b64_e32 v[60:61], 0
	v_mov_b64_e32 v[62:63], 0
	v_mov_b64_e32 v[64:65], 0
	v_mov_b64_e32 v[66:67], 0
	v_mov_b64_e32 v[68:69], 0
	v_mov_b64_e32 v[70:71], 0
	v_mov_b64_e32 v[72:73], 0
	v_mov_b64_e32 v[74:75], 0
	v_mov_b64_e32 v[76:77], 0
	v_mov_b64_e32 v[78:79], 0
	v_mov_b64_e32 v[80:81], 0
	v_mov_b64_e32 v[82:83], 0
	v_mov_b64_e32 v[84:85], 0
	v_mov_b64_e32 v[86:87], 0
	v_mov_b64_e32 v[88:89], 0
	v_mov_b64_e32 v[90:91], 0
	v_mov_b64_e32 v[92:93], 0
	v_mov_b64_e32 v[94:95], 0
	v_mov_b64_e32 v[96:97], 0
	v_mov_b64_e32 v[98:99], 0
	v_mov_b64_e32 v[100:101], 0
	v_mov_b64_e32 v[102:103], 0
	v_mov_b64_e32 v[104:105], 0
	v_mov_b64_e32 v[106:107], 0
	v_mov_b64_e32 v[108:109], 0
	v_mov_b64_e32 v[110:111], 0
	v_mov_b64_e32 v[112:113], 0
	v_mov_b64_e32 v[114:115], 0
	v_mov_b64_e32 v[116:117], 0
	v_mov_b64_e32 v[118:119], 0
	v_mov_b64_e32 v[120:121], 0
	v_mov_b64_e32 v[122:123], 0
	v_mov_b64_e32 v[124:125], 0
	v_mov_b64_e32 v[126:127], 0
